# v33
# speedup vs baseline: 1.1217x; 1.0053x over previous
.LBB1_73:
	s_or_b64 exec, exec, s[0:1]
	v_cmp_gt_u32_e32 vcc, 64, v0
	s_waitcnt lgkmcnt(0)
	s_barrier
	s_and_saveexec_b64 s[0:1], vcc
	s_cbranch_execz .LBB1_75
	v_lshlrev_b32_e32 v3, 2, v110
	ds_read_b128 v[4:7], v3 offset:8320
	s_waitcnt lgkmcnt(0)
	v_add_u32_e32 v11, v5, v4
	v_add3_u32 v7, v11, v6, v7
	v_mov_b32_e32 v8, v7
	s_nop 1
	v_add_u32_dpp v8, v8, v8 row_shr:1 row_mask:0xf bank_mask:0xf bound_ctrl:1
	s_nop 1
	v_add_u32_dpp v8, v8, v8 row_shr:2 row_mask:0xf bank_mask:0xf bound_ctrl:1
	s_nop 1
	v_add_u32_dpp v8, v8, v8 row_shr:4 row_mask:0xf bank_mask:0xf bound_ctrl:1
	s_nop 1
	v_add_u32_dpp v8, v8, v8 row_shr:8 row_mask:0xf bank_mask:0xf bound_ctrl:1
	s_nop 1
	v_add_u32_dpp v8, v8, v8 row_bcast:15 row_mask:0xa bank_mask:0xf
	s_nop 1
	v_add_u32_dpp v8, v8, v8 row_bcast:31 row_mask:0xc bank_mask:0xf
	v_sub_u32_e32 v8, v8, v7
	v_add_u32_e32 v9, v8, v4
	v_add_u32_e32 v10, v9, v5
	v_add_u32_e32 v11, v10, v6
	ds_write_b128 v3, v[8:11] offset:8320

.LBB2_18:
	s_or_b64 exec, exec, s[18:19]
	v_cmp_gt_u32_e64 s[0:1], 64, v0
	s_waitcnt lgkmcnt(0)
	s_barrier
	s_and_saveexec_b64 s[18:19], s[0:1]
	s_cbranch_execz .LBB2_20
	v_lshlrev_b32_e32 v4, 4, v0
	ds_read_b128 v[10:13], v4 offset:1024
	s_waitcnt lgkmcnt(0)
	v_add_u32_e32 v15, v11, v10
	v_add3_u32 v13, v15, v12, v13
	v_mov_b32_e32 v5, v13
	s_nop 1
	v_add_u32_dpp v5, v5, v5 row_shr:1 row_mask:0xf bank_mask:0xf bound_ctrl:1
	s_nop 1
	v_add_u32_dpp v5, v5, v5 row_shr:2 row_mask:0xf bank_mask:0xf bound_ctrl:1
	s_nop 1
	v_add_u32_dpp v5, v5, v5 row_shr:4 row_mask:0xf bank_mask:0xf bound_ctrl:1
	s_nop 1
	v_add_u32_dpp v5, v5, v5 row_shr:8 row_mask:0xf bank_mask:0xf bound_ctrl:1
	s_nop 1
	v_add_u32_dpp v5, v5, v5 row_bcast:15 row_mask:0xa bank_mask:0xf
	s_nop 1
	v_add_u32_dpp v5, v5, v5 row_bcast:31 row_mask:0xc bank_mask:0xf
	v_sub_u32_e32 v14, v5, v13
	v_add_u32_e32 v15, v14, v10
	v_add_u32_e32 v16, v15, v11
	v_add_u32_e32 v17, v16, v12
	ds_write_b128 v4, v[14:17] offset:2048
